# relative-bias score tables built at the end of P1 by the last 16 workgroups (one unit fewer, otherwise idle at the barrier) instead of at kernel start by workgroups 0..8
# speedup vs baseline: 1.0004x; 1.0004x over previous
.Lplace_ok:
.LBB0_13:
	s_or_b64 exec, exec, s[0:1]
	s_add_u32 s72, s90, 0x100000
	s_addc_u32 s73, s91, 0
	s_add_u32 s70, s90, 0xe00000
	s_addc_u32 s71, s91, 0
	s_add_u32 s0, s90, 0xd800000
	s_addc_u32 s1, s91, 0
	s_add_u32 s74, s90, 0x200000
	v_writelane_b32 v255, s0, 14
	s_addc_u32 s75, s91, 0
	s_nop 0
	v_writelane_b32 v255, s1, 15
	s_add_u32 s0, s90, 0x1100000
	s_addc_u32 s1, s91, 0
	v_writelane_b32 v255, s0, 16
	s_nop 1
	v_writelane_b32 v255, s1, 17
	s_lshr_b32 s0, s10, 6
	v_readlane_b32 s5, v255, 2
	s_abs_i32 s94, s5
	v_cvt_f32_u32_e32 v1, s94
	s_sub_i32 s2, 0, s94
	v_writelane_b32 v255, s0, 18
	s_add_i32 s0, s5, 0xfff
	v_rcp_iflag_f32_e32 v1, v1
	s_ashr_i32 s1, s0, 31
	s_abs_i32 s0, s0
	s_ashr_i32 s6, s5, 31
	v_mul_f32_e32 v1, 0x4f7ffffe, v1
	v_cvt_u32_f32_e32 v1, v1
	s_xor_b32 s1, s1, s6
	v_writelane_b32 v255, s6, 19
	v_readfirstlane_b32 s3, v1
	s_mul_i32 s2, s2, s3
	s_mul_hi_u32 s2, s3, s2
	s_add_i32 s96, s3, s2
	s_mul_hi_u32 s2, s0, s96
	s_mul_i32 s3, s2, s94
	s_sub_i32 s0, s0, s3
	s_add_i32 s4, s2, 1
	s_sub_i32 s3, s0, s94
	s_cmp_ge_u32 s0, s94
	s_cselect_b32 s2, s4, s2
	s_cselect_b32 s0, s3, s0
	s_add_i32 s3, s2, 1
	s_cmp_ge_u32 s0, s94
	s_cselect_b32 s0, s3, s2
	s_xor_b32 s0, s0, s1
	s_sub_i32 s33, s0, s1
	s_add_i32 s0, s5, 0xbfff
	s_ashr_i32 s1, s0, 31
	s_abs_i32 s0, s0
	s_mul_hi_u32 s2, s0, s96
	s_mul_i32 s3, s2, s94
	s_sub_i32 s0, s0, s3
	s_xor_b32 s1, s1, s6
	s_add_i32 s3, s2, 1
	s_sub_i32 s4, s0, s94
	s_cmp_ge_u32 s0, s94
	s_cselect_b32 s2, s3, s2
	s_cselect_b32 s0, s4, s0
	s_add_i32 s3, s2, 1
	s_cmp_ge_u32 s0, s94
	s_cselect_b32 s0, s3, s2
	s_xor_b32 s0, s0, s1
	s_sub_i32 s0, s0, s1
	s_min_i32 s34, s0, 0
	s_add_i32 s34, s34, s33
	s_cmp_lt_i32 s80, 1
	v_writelane_b32 v255, s0, 20
	s_cselect_b64 s[0:1], -1, 0
	s_cmp_gt_i32 s81, 0
	s_cselect_b64 s[2:3], -1, 0
	v_writelane_b32 v255, s90, 21
	s_and_b64 s[68:69], s[0:1], s[2:3]
	s_mov_b64 s[0:1], s[80:81]
	v_writelane_b32 v255, s91, 22
	v_writelane_b32 v255, s0, 23
	s_andn2_b64 vcc, exec, s[68:69]
	v_and_b32_e32 v1, 63, v0
	v_writelane_b32 v255, s1, 24
	v_writelane_b32 v255, s2, 25
	v_writelane_b32 v255, s3, 26
	v_writelane_b32 v255, s10, 27
	s_cbranch_vccnz .LBB0_220
	v_readlane_b32 s0, v255, 2
	s_lshl_b32 s4, s0, 2
	s_abs_i32 s2, s4
	v_cvt_f32_u32_e32 v2, s2
	s_add_i32 s5, s4, 0x3fff
	s_abs_i32 s3, s5
	v_rcp_iflag_f32_e32 v3, v2
	s_sub_i32 s0, 0, s2
	v_mul_f32_e32 v3, 0x4f7ffffe, v3
	v_cvt_u32_f32_e32 v3, v3
	s_nop 0
	v_readfirstlane_b32 s6, v3
	s_mul_i32 s0, s0, s6
	s_mul_hi_u32 s0, s6, s0
	s_add_i32 s6, s6, s0
	s_mul_hi_u32 s6, s3, s6
	s_ashr_i32 s5, s5, 31
	s_ashr_i32 s4, s4, 31
	s_mov_b64 s[0:1], exec
	v_readlane_b32 s8, v255, 12
	v_readlane_b32 s9, v255, 13
	s_and_b64 s[8:9], s[0:1], s[8:9]
	s_mov_b64 exec, s[8:9]
	s_add_i32 s7, 0, 0x20280
	v_mov_b32_e32 v2, 0
	v_mov_b32_e32 v3, v2
	v_mov_b32_e32 v4, s7
	ds_write_b64 v4, v[2:3]
	s_or_b64 exec, exec, s[0:1]
	s_mul_i32 s1, s6, s2
	s_sub_i32 s1, s3, s1
	s_xor_b32 s0, s5, s4
	s_add_i32 s3, s6, 1
	s_sub_i32 s4, s1, s2
	s_cmp_ge_u32 s1, s2
	s_cselect_b32 s3, s3, s6
	s_cselect_b32 s1, s4, s1
	s_add_i32 s4, s3, 1
	s_cmp_ge_u32 s1, s2
	s_cselect_b32 s1, s4, s3
	s_xor_b32 s1, s1, s0
	s_sub_i32 s35, s1, s0
	s_cmp_gt_i32 s35, 0
	s_cselect_b64 s[76:77], -1, 0
	s_cmp_gt_i32 s34, 0
	s_cselect_b64 s[78:79], -1, 0
	s_or_b64 s[0:1], s[78:79], s[76:77]
	s_mov_b32 s23, 0
	s_andn2_b64 vcc, exec, s[0:1]
	s_waitcnt lgkmcnt(0)
	s_barrier
	s_cbranch_vccnz .LBB0_219
	v_readlane_b32 s0, v255, 18
	s_mulk_i32 s0, 0x2100
	v_lshrrev_b32_e32 v98, 3, v1
	v_and_b32_e32 v4, 7, v0
	s_add_i32 s0, s0, 0
	v_readlane_b32 s2, v255, 8
	v_mul_u32_u24_e32 v3, 0x84, v98
	v_lshlrev_b32_e32 v5, 4, v4
	s_cmpk_lt_u32 s10, 0x100
	s_mul_i32 s1, s2, s35
	v_add3_u32 v99, s0, v3, v5
	v_lshlrev_b32_e32 v102, 3, v4
	v_mul_u32_u24_e32 v3, 0x420, v4
	v_lshlrev_b32_e32 v4, 2, v98
	s_cselect_b64 s[80:81], -1, 0
	s_lshl_b32 s66, s1, 2
	v_mov_b32_e32 v101, 0
	v_lshlrev_b32_e32 v2, 2, v0
	v_add3_u32 v105, s0, v3, v4
	v_lshlrev_b32_e32 v100, 4, v1
	v_readlane_b32 s0, v255, 14
	v_and_b32_e32 v2, 28, v2
	v_lshl_add_u64 v[110:111], s[14:15], 0, v[100:101]
	v_lshl_add_u64 v[112:113], s[12:13], 0, v[100:101]
	v_lshlrev_b32_e32 v100, 2, v1
	v_readlane_b32 s1, v255, 15
	s_add_u32 s82, s90, 0xe00400
	v_cmp_eq_u32_e64 s[6:7], 0, v1
	v_lshl_add_u64 v[114:115], s[0:1], 0, v[100:101]
	v_lshlrev_b32_e32 v100, 2, v2
	v_mbcnt_lo_u32_b32 v2, -1, 0
	s_mul_i32 s67, s33, s2
	s_addc_u32 s83, s91, 0
	v_mov_b32_e32 v103, v101
	v_or_b32_e32 v104, 8, v98
	v_or_b32_e32 v106, 16, v98
	v_or_b32_e32 v108, 24, v98
	s_add_i32 s90, 0, 0x20284
	s_add_i32 s91, 0, 0x20280
	v_mov_b32_e32 v107, 0x3727c5ac
	s_mov_b32 s92, 0xf800000
	v_mov_b32_e32 v109, 0x260
	v_mbcnt_hi_u32_b32 v116, -1, v2
	s_branch .LBB0_23

.LBB0_364:
	s_cmp_gt_i32 s81, 2
	s_cselect_b64 s[0:1], -1, 0
	s_and_b64 s[2:3], s[22:23], s[0:1]
	s_andn2_b64 vcc, exec, s[2:3]
	s_cbranch_vccnz .LBB0_416
	v_readlane_b32 s2, v255, 7
	v_readlane_b32 s3, v255, 2
	s_sub_i32 s2, s2, s3
	s_add_i32 s2, s2, 16
	s_cmp_lt_i32 s2, 0
	s_cbranch_scc1 .Ltab_done
	v_readlane_b32 s4, v255, 0
	v_readlane_b32 s5, v255, 1
	s_sub_u32 s4, s4, 0xb8
	s_subb_u32 s5, s5, 0
	s_load_dwordx2 s[22:23], s[4:5], 0x28
	v_lshl_or_b32 v70, s2, 9, v0
	s_movk_i32 s9, 0x1010
	v_cmp_gt_i32_e32 vcc, s9, v70
	s_waitcnt lgkmcnt(0)
	s_and_saveexec_b64 s[6:7], vcc
	s_cbranch_execz .Ltab_a_done
	s_mov_b32 s8, 0x7f807f81
	v_mul_hi_i32 v71, v70, s8
	v_lshrrev_b32_e32 v72, 31, v71
	v_ashrrev_i32_e32 v71, 7, v71
	v_add_u32_e32 v71, v71, v72
	v_mul_i32_i24_e32 v72, 0x101, v71
	v_sub_u32_e32 v72, v70, v72
	v_ashrrev_i32_e32 v73, 31, v72
	s_getpc_b64 s[10:11]
	s_add_u32 s10, s10, _ZL5BKT_A@rel32@lo+4
	s_addc_u32 s11, s11, _ZL5BKT_A@rel32@hi+12
	v_lshl_add_u64 v[74:75], s[10:11], 0, v[72:73]
	global_load_ubyte v74, v[74:75], off
	s_movk_i32 s8, 0x404
	s_waitcnt vmcnt(0)
	v_mad_u32_u24 v74, v74, 28, v71
	v_ashrrev_i32_e32 v75, 31, v74
	v_lshl_add_u64 v[74:75], v[74:75], 2, s[22:23]
	global_load_dword v76, v[74:75], off
	v_mov_b64_e32 v[74:75], s[72:73]
	v_mad_i64_i32 v[74:75], s[10:11], v71, s8, v[74:75]
	v_lshl_add_u64 v[72:73], v[72:73], 2, v[74:75]
	s_waitcnt vmcnt(0)
	global_store_dword v[72:73], v76, off
.Ltab_a_done:
	s_or_b64 exec, exec, s[6:7]
	s_movk_i32 s9, 0x60c
	v_cmp_gt_i32_e32 vcc, s9, v70
	s_and_saveexec_b64 s[6:7], vcc
	s_cbranch_execz .Ltab_b_done
	s_mov_b32 s8, 0xfe03f81
	v_mul_hi_i32 v71, v70, s8
	v_ashrrev_i32_e32 v72, 5, v71
	v_lshrrev_b32_e32 v73, 31, v71
	v_ashrrev_i32_e32 v71, 3, v71
	v_add_u32_e32 v76, v71, v73
	v_lshl_add_u32 v71, v76, 7, v76
	s_getpc_b64 s[10:11]
	s_add_u32 s10, s10, _ZL5BKT_B@rel32@lo+4
	s_addc_u32 s11, s11, _ZL5BKT_B@rel32@hi+12
	v_add_u32_e32 v78, v72, v73
	v_sub_u32_e32 v70, v70, v71
	s_movk_i32 s8, 0x81
	v_mov_b64_e32 v[72:73], s[10:11]
	v_mad_i64_i32 v[72:73], s[10:11], v78, s8, v[72:73]
	v_ashrrev_i32_e32 v71, 31, v70
	v_lshl_add_u64 v[72:73], v[72:73], 0, v[70:71]
	global_load_ubyte v72, v[72:73], off
	v_lshrrev_b32_e32 v75, 30, v76
	v_add_u32_e32 v77, v76, v75
	v_and_b32_e32 v77, -4, v77
	v_lshlrev_b32_e32 v74, 2, v78
	v_sub_u32_e32 v76, v76, v77
	v_ashrrev_i32_e32 v75, 31, v74
	v_ashrrev_i32_e32 v77, 31, v76
	v_mov_b32_e32 v73, 0
	v_lshl_add_u64 v[74:75], v[74:75], 0, v[76:77]
	s_movk_i32 s8, 0x810
	s_waitcnt vmcnt(0)
	v_mul_u32_u24_e32 v72, 28, v72
	v_lshl_add_u64 v[72:73], v[74:75], 0, v[72:73]
	v_lshl_add_u64 v[72:73], v[72:73], 2, s[22:23]
	global_load_dword v74, v[72:73], off offset:64
	v_mov_b64_e32 v[72:73], s[90:91]
	v_mad_i64_i32 v[72:73], s[10:11], v78, s8, v[72:73]
	s_mov_b64 s[10:11], 0x104040
	s_nop 0
	v_lshl_add_u64 v[72:73], v[72:73], 0, s[10:11]
	s_movk_i32 s8, 0x204
	v_mad_i64_i32 v[72:73], s[10:11], v76, s8, v[72:73]
	v_lshl_add_u64 v[70:71], v[70:71], 2, v[72:73]
	s_waitcnt vmcnt(0)
	global_store_dword v[70:71], v74, off

.Ltab_done:
	s_waitcnt vmcnt(0)
	s_waitcnt vmcnt(0) lgkmcnt(0)
	s_barrier
	s_mov_b64 s[4:5], exec
	v_readlane_b32 s2, v255, 12
	v_readlane_b32 s3, v255, 13
	s_and_b64 s[2:3], s[4:5], s[2:3]
	s_mov_b64 exec, s[2:3]
	s_cbranch_execz .LBB0_415
	s_add_i32 s2, 0, 0x20160
	v_mov_b32_e32 v2, s2
	s_waitcnt vmcnt(0) expcnt(0) lgkmcnt(0)
	ds_read_b32 v4, v2
	s_add_i32 s2, 0, 0x20164
	v_mov_b32_e32 v2, s2
	ds_read_b32 v2, v2
	s_waitcnt lgkmcnt(1)
	v_cmp_ne_u32_e32 vcc, 0, v4
	s_cbranch_vccnz .LBB0_381
	v_readlane_b32 s2, v255, 0
	v_readlane_b32 s3, v255, 1
	s_load_dwordx2 s[8:9], s[2:3], 0x4
	v_readlane_b32 s14, v255, 9
	v_readlane_b32 s15, v255, 10
	s_add_u32 s2, s14, 0x1000
	s_addc_u32 s3, s15, 0
	s_add_u32 s6, s14, 0x1100
	s_addc_u32 s7, s15, 0
	v_readlane_b32 s10, v255, 2
	s_waitcnt lgkmcnt(0)
	s_mul_i32 s10, s8, s10
	s_add_u32 s8, s14, 0x1200
	s_mul_i32 s10, s10, s9
	s_addc_u32 s9, s15, 0
	s_add_u32 s18, s14, 0x1300
	s_addc_u32 s19, s15, 0
	s_mov_b32 s11, 1
	v_mov_b32_e32 v18, 0
	s_branch .LBB0_369
